# NA attention: the two low 3-bit fields of bid swapped, so an XCD owns groups of 4 consecutive block rows (both head halves)
# speedup vs baseline: 1.0048x; 1.0048x over previous
; __device__ __forceinline__ void phase_na_attention(const Params& P, float* sm, int bid, int nb) {
;     ...
;     const int lane = threadIdx.x & 63, wave = threadIdx.x >> 6, r = lane & 31, h = lane >> 5;
;     const float SC = 0.125f * 1.4426950408889634f, L2E = 1.4426950408889634f;
;     __syncthreads();
;     for (int e = threadIdx.x; e < 8 * 15 * 31; e += NTHR) sm[e] = P.in[12][e] * L2E;
;     __syncthreads();
;     for (int task = bid * 8 + wave; task < 260 * 16; task += nb * 8) {
;         const int qh = task & 1, head = (task >> 1) & 7, blk = task >> 4;
;         const bool lat = blk >= 4;
;         const int rr = blk - 4;
;         const int tok = blk * 64 + qh * 32 + r;
;         const int c = qh * 32 + r;
;         const int cs = min(max(c - 8, 0), 48), rs = min(max(rr - 4, 0), 248);
.LBB0_485:
	s_or_b64 exec, exec, s[0:1]
	s_mov_b32 s0, s44
	v_and_b32_e32 v180, 31, v0
	v_lshrrev_b32_e32 v2, 6, v0
	v_writelane_b32 v252, s0, 23
	v_readlane_b32 s96, v253, 10
	s_cmpk_lg_u32 s96, 0x100
	s_mov_b32 s96, s44
	s_cbranch_scc1 .Lna_sw3
	s_and_b32 s96, s44, 0xc0
	s_and_b32 s97, s44, 7
	s_lshl_b32 s97, s97, 3
	s_or_b32 s96, s96, s97
	s_bfe_u32 s97, s44, 0x30003
	s_or_b32 s96, s96, s97
